# baseline (speedup 1.0000x reference)
.Lca_ok_1:
	buffer_load_dwordx4 v[42:45], v117, s[4:7], 0 offen offset:0 sc1
	ds_read_b128 v[50:53], v116 offset:256
	s_setprio 0
	v_exp_f32_e32 v94, v86
	v_exp_f32_e32 v95, v90
	v_exp_f32_e32 v96, v84
	v_exp_f32_e32 v97, v88
	v_exp_f32_e32 v98, v85
	v_exp_f32_e32 v99, v89
	v_pk_add_f32 v[100:101], v[94:95], 1.0 op_sel_hi:[1,0]
	v_pk_fma_f32 v[102:103], v[94:95], s[8:9], v[92:93] op_sel_hi:[1,0,0]
	v_pk_fma_f32 v[100:101], v[96:97], v[100:101], v[100:101]
	v_pk_fma_f32 v[104:105], v[100:101], v[98:99], v[100:101]
	v_rcp_f32_e32 v104, v104
	v_rcp_f32_e32 v105, v105
	v_pk_fma_f32 v[102:103], v[102:103], v[98:99], v[102:103]
	v_pk_fma_f32 v[102:103], v[64:65], v[100:101], v[102:103]
	v_exp_f32_e32 v106, v87
	v_pk_mul_f32 v[64:65], v[102:103], v[104:105]
	v_exp_f32_e32 v108, v64
	v_exp_f32_e32 v109, v65
	v_exp_f32_e32 v107, v91
	v_pk_add_f32 v[110:111], v[108:109], 1.0 op_sel_hi:[1,0]
	v_pk_fma_f32 v[110:111], v[110:111], v[106:107], v[110:111]
	v_rcp_f32_e32 v110, v110
	v_rcp_f32_e32 v111, v111
	v_pk_add_f32 v[112:113], v[108:109], -1.0 op_sel_hi:[1,0]
	v_pk_mul_f32 v[112:113], v[112:113], v[110:111]
	v_cvt_pk_f16_f32 v114, v112, v113
	ds_write_b32 v81, v114 offset:0
	s_waitcnt lgkmcnt(0)
	global_load_dword v67, v66, s[0:1] sc1
	global_load_dword v68, v66, s[0:1] offset:4 sc1
	s_waitcnt vmcnt(3)
	s_setprio 2
	s_barrier
	v_mfma_f32_16x16x32_f16 v[84:87], v[6:9], v[50:53], v[18:21]
	v_mfma_f32_16x16x32_f16 v[88:91], v[10:13], v[50:53], v[38:41]
	ds_read_b128 v[56:59], v75 offset:0
	ds_read_b128 v[60:63], v75 offset:1024
	v_mfma_f32_16x16x32_f16 v[84:87], v[2:5], v[46:49], v[84:87]
	v_mfma_f32_16x16x32_f16 v[88:91], v[14:17], v[46:49], v[88:91]
	s_waitcnt lgkmcnt(1)
	v_mfma_f32_16x16x32_f16 v[84:87], v[30:33], v[56:59], v[84:87]
	v_mfma_f32_16x16x32_f16 v[88:91], v[22:25], v[56:59], v[88:91]
	s_waitcnt lgkmcnt(0)
	v_mfma_f32_16x16x32_f16 v[84:87], v[34:37], v[60:63], v[84:87]
	v_mfma_f32_16x16x32_f16 v[88:91], v[26:29], v[60:63], v[88:91]
	s_add_u32 s13, s12, 4
	s_min_u32 s13, s13, 450
	s_cmp_ge_u32 s14, s13
	s_cbranch_scc0 .Lca_slow_6
.Lca_ok_4:
	buffer_load_dwordx4 v[46:49], v117, s[4:7], 0 offen offset:1024 sc1
	ds_read_b128 v[50:53], v116 offset:512
	s_setprio 0
	v_exp_f32_e32 v94, v86
	v_exp_f32_e32 v95, v90
	v_exp_f32_e32 v96, v84
	v_exp_f32_e32 v97, v88
	v_exp_f32_e32 v98, v85
	v_exp_f32_e32 v99, v89
	v_pk_add_f32 v[100:101], v[94:95], 1.0 op_sel_hi:[1,0]
	v_pk_fma_f32 v[102:103], v[94:95], s[8:9], v[92:93] op_sel_hi:[1,0,0]
	v_pk_fma_f32 v[100:101], v[96:97], v[100:101], v[100:101]
	v_pk_fma_f32 v[104:105], v[100:101], v[98:99], v[100:101]
	v_rcp_f32_e32 v104, v104
	v_rcp_f32_e32 v105, v105
	v_pk_fma_f32 v[102:103], v[102:103], v[98:99], v[102:103]
	v_pk_fma_f32 v[102:103], v[64:65], v[100:101], v[102:103]
	v_exp_f32_e32 v106, v87
	v_pk_mul_f32 v[64:65], v[102:103], v[104:105]
	v_exp_f32_e32 v108, v64
	v_exp_f32_e32 v109, v65
	v_exp_f32_e32 v107, v91
	v_pk_add_f32 v[110:111], v[108:109], 1.0 op_sel_hi:[1,0]
	v_pk_fma_f32 v[110:111], v[110:111], v[106:107], v[110:111]
	v_rcp_f32_e32 v110, v110
	v_rcp_f32_e32 v111, v111
	v_pk_add_f32 v[112:113], v[108:109], -1.0 op_sel_hi:[1,0]
	v_pk_mul_f32 v[112:113], v[112:113], v[110:111]
	v_cvt_pk_f16_f32 v114, v112, v113
	ds_write_b32 v81, v114 offset:2048
	s_waitcnt lgkmcnt(0)
	s_waitcnt vmcnt(3)
	v_add_u32_e32 v116, 0x200, v116
	v_add_u32_e32 v117, 0x800, v117
	s_mov_b32 s12, 2
	.p2align	6
.Lca_loop:
	s_setprio 2
	s_barrier
	v_mfma_f32_16x16x32_f16 v[84:87], v[6:9], v[50:53], v[18:21]
	v_mfma_f32_16x16x32_f16 v[88:91], v[10:13], v[50:53], v[38:41]
	ds_read_b128 v[56:59], v75 offset:2048
	ds_read_b128 v[60:63], v75 offset:3072
	v_mfma_f32_16x16x32_f16 v[84:87], v[2:5], v[42:45], v[84:87]
	v_mfma_f32_16x16x32_f16 v[88:91], v[14:17], v[42:45], v[88:91]
	s_waitcnt lgkmcnt(1)
	v_mfma_f32_16x16x32_f16 v[84:87], v[30:33], v[56:59], v[84:87]
	v_mfma_f32_16x16x32_f16 v[88:91], v[22:25], v[56:59], v[88:91]
	s_waitcnt lgkmcnt(0)
	v_mfma_f32_16x16x32_f16 v[84:87], v[34:37], v[60:63], v[84:87]
	v_mfma_f32_16x16x32_f16 v[88:91], v[26:29], v[60:63], v[88:91]
	s_add_u32 s13, s12, 3
	s_min_u32 s13, s13, 450
	s_cmp_ge_u32 s14, s13
	s_cbranch_scc0 .Lca_slow_9
.Lca_ok_7:
	buffer_load_dwordx4 v[42:45], v117, s[4:7], 0 offen offset:0 sc1
	ds_read_b128 v[50:53], v116 offset:256
	s_setprio 0
	v_min_f32_e32 v64, 0x42700000, v64
	v_min_f32_e32 v65, 0x42700000, v65
	v_exp_f32_e32 v94, v86
	v_exp_f32_e32 v95, v90
	v_exp_f32_e32 v96, v84
	v_exp_f32_e32 v97, v88
	v_exp_f32_e32 v98, v85
	v_exp_f32_e32 v99, v89
	v_pk_add_f32 v[100:101], v[94:95], 1.0 op_sel_hi:[1,0]
	v_pk_fma_f32 v[102:103], v[94:95], s[8:9], v[92:93] op_sel_hi:[1,0,0]
	v_pk_fma_f32 v[100:101], v[96:97], v[100:101], v[100:101]
	v_pk_fma_f32 v[104:105], v[100:101], v[98:99], v[100:101]
	v_rcp_f32_e32 v104, v104
	v_rcp_f32_e32 v105, v105
	v_pk_fma_f32 v[102:103], v[102:103], v[98:99], v[102:103]
	v_pk_fma_f32 v[102:103], v[64:65], v[100:101], v[102:103]
	v_exp_f32_e32 v106, v87
	v_pk_mul_f32 v[64:65], v[102:103], v[104:105]
	v_exp_f32_e32 v108, v64
	v_exp_f32_e32 v109, v65
	v_exp_f32_e32 v107, v91
	v_pk_add_f32 v[110:111], v[108:109], 1.0 op_sel_hi:[1,0]
	v_pk_fma_f32 v[110:111], v[110:111], v[106:107], v[110:111]
	v_rcp_f32_e32 v110, v110
	v_rcp_f32_e32 v111, v111
	v_pk_add_f32 v[112:113], v[108:109], -1.0 op_sel_hi:[1,0]
	v_pk_mul_f32 v[112:113], v[112:113], v[110:111]
	v_cvt_pk_f16_f32 v114, v112, v113
	ds_write_b32 v81, v114 offset:0
	s_waitcnt lgkmcnt(0)
	s_waitcnt vmcnt(2)
	v_readfirstlane_b32 s10, v67
	v_readfirstlane_b32 s11, v68
	global_load_dword v67, v66, s[0:1] sc1
	global_load_dword v68, v66, s[0:1] offset:4 sc1
	s_min_u32 s10, s10, s11
	s_max_u32 s14, s14, s10
	s_waitcnt vmcnt(3)
	s_setprio 2
	s_barrier
	v_mfma_f32_16x16x32_f16 v[84:87], v[6:9], v[50:53], v[18:21]
	v_mfma_f32_16x16x32_f16 v[88:91], v[10:13], v[50:53], v[38:41]
	ds_read_b128 v[56:59], v75 offset:0
	ds_read_b128 v[60:63], v75 offset:1024
	v_mfma_f32_16x16x32_f16 v[84:87], v[2:5], v[46:49], v[84:87]
	v_mfma_f32_16x16x32_f16 v[88:91], v[14:17], v[46:49], v[88:91]
	s_waitcnt lgkmcnt(1)
	v_mfma_f32_16x16x32_f16 v[84:87], v[30:33], v[56:59], v[84:87]
	v_mfma_f32_16x16x32_f16 v[88:91], v[22:25], v[56:59], v[88:91]
	s_waitcnt lgkmcnt(0)
	v_mfma_f32_16x16x32_f16 v[84:87], v[34:37], v[60:63], v[84:87]
	v_mfma_f32_16x16x32_f16 v[88:91], v[26:29], v[60:63], v[88:91]
	s_add_u32 s13, s12, 4
	s_min_u32 s13, s13, 450
	s_cmp_ge_u32 s14, s13
	s_cbranch_scc0 .Lca_slow_12
.Lca_ok_10:
	buffer_load_dwordx4 v[46:49], v117, s[4:7], 0 offen offset:1024 sc1
	ds_read_b128 v[50:53], v116 offset:512
	s_setprio 0
	v_exp_f32_e32 v94, v86
	v_exp_f32_e32 v95, v90
	v_exp_f32_e32 v96, v84
	v_exp_f32_e32 v97, v88
	v_exp_f32_e32 v98, v85
	v_exp_f32_e32 v99, v89
	v_pk_add_f32 v[100:101], v[94:95], 1.0 op_sel_hi:[1,0]
	v_pk_fma_f32 v[102:103], v[94:95], s[8:9], v[92:93] op_sel_hi:[1,0,0]
	v_pk_fma_f32 v[100:101], v[96:97], v[100:101], v[100:101]
	v_pk_fma_f32 v[104:105], v[100:101], v[98:99], v[100:101]
	v_rcp_f32_e32 v104, v104
	v_rcp_f32_e32 v105, v105
	v_pk_fma_f32 v[102:103], v[102:103], v[98:99], v[102:103]
	v_pk_fma_f32 v[102:103], v[64:65], v[100:101], v[102:103]
	v_exp_f32_e32 v106, v87
	v_pk_mul_f32 v[64:65], v[102:103], v[104:105]
	v_exp_f32_e32 v108, v64
	v_exp_f32_e32 v109, v65
	v_exp_f32_e32 v107, v91
	v_pk_add_f32 v[110:111], v[108:109], 1.0 op_sel_hi:[1,0]
	v_pk_fma_f32 v[110:111], v[110:111], v[106:107], v[110:111]
	v_rcp_f32_e32 v110, v110
	v_rcp_f32_e32 v111, v111
	v_pk_add_f32 v[112:113], v[108:109], -1.0 op_sel_hi:[1,0]
	v_pk_mul_f32 v[112:113], v[112:113], v[110:111]
	v_cvt_pk_f16_f32 v114, v112, v113
	ds_write_b32 v81, v114 offset:2048
	s_waitcnt lgkmcnt(0)
	s_waitcnt vmcnt(3)
	s_setprio 2
	s_barrier
	v_mfma_f32_16x16x32_f16 v[84:87], v[6:9], v[50:53], v[18:21]
	v_mfma_f32_16x16x32_f16 v[88:91], v[10:13], v[50:53], v[38:41]
	ds_read_b128 v[56:59], v75 offset:2048
	ds_read_b128 v[60:63], v75 offset:3072
	v_mfma_f32_16x16x32_f16 v[84:87], v[2:5], v[42:45], v[84:87]
	v_mfma_f32_16x16x32_f16 v[88:91], v[14:17], v[42:45], v[88:91]
	s_waitcnt lgkmcnt(1)
	v_mfma_f32_16x16x32_f16 v[84:87], v[30:33], v[56:59], v[84:87]
	v_mfma_f32_16x16x32_f16 v[88:91], v[22:25], v[56:59], v[88:91]
	s_waitcnt lgkmcnt(0)
	v_mfma_f32_16x16x32_f16 v[84:87], v[34:37], v[60:63], v[84:87]
	v_mfma_f32_16x16x32_f16 v[88:91], v[26:29], v[60:63], v[88:91]
	s_add_u32 s13, s12, 5
	s_min_u32 s13, s13, 450
	s_cmp_ge_u32 s14, s13
	s_cbranch_scc0 .Lca_slow_15
.Lca_ok_13:
	buffer_load_dwordx4 v[42:45], v117, s[4:7], 0 offen offset:2048 sc1
	ds_read_b128 v[50:53], v116 offset:768
	s_setprio 0
	v_exp_f32_e32 v94, v86
	v_exp_f32_e32 v95, v90
	v_exp_f32_e32 v96, v84
	v_exp_f32_e32 v97, v88
	v_exp_f32_e32 v98, v85
	v_exp_f32_e32 v99, v89
	v_pk_add_f32 v[100:101], v[94:95], 1.0 op_sel_hi:[1,0]
	v_pk_fma_f32 v[102:103], v[94:95], s[8:9], v[92:93] op_sel_hi:[1,0,0]
	v_pk_fma_f32 v[100:101], v[96:97], v[100:101], v[100:101]
	v_pk_fma_f32 v[104:105], v[100:101], v[98:99], v[100:101]
	v_rcp_f32_e32 v104, v104
	v_rcp_f32_e32 v105, v105
	v_pk_fma_f32 v[102:103], v[102:103], v[98:99], v[102:103]
	v_pk_fma_f32 v[102:103], v[64:65], v[100:101], v[102:103]
	v_exp_f32_e32 v106, v87
	v_pk_mul_f32 v[64:65], v[102:103], v[104:105]
	v_exp_f32_e32 v108, v64
	v_exp_f32_e32 v109, v65
	v_exp_f32_e32 v107, v91
	v_pk_add_f32 v[110:111], v[108:109], 1.0 op_sel_hi:[1,0]
	v_pk_fma_f32 v[110:111], v[110:111], v[106:107], v[110:111]
	v_rcp_f32_e32 v110, v110
	v_rcp_f32_e32 v111, v111
	v_pk_add_f32 v[112:113], v[108:109], -1.0 op_sel_hi:[1,0]
	v_pk_mul_f32 v[112:113], v[112:113], v[110:111]
	v_cvt_pk_f16_f32 v114, v112, v113
	ds_write_b32 v81, v114 offset:0
	s_waitcnt lgkmcnt(0)
	s_waitcnt vmcnt(2)
	v_readfirstlane_b32 s10, v67
	v_readfirstlane_b32 s11, v68
	global_load_dword v67, v66, s[0:1] sc1
	global_load_dword v68, v66, s[0:1] offset:4 sc1
	s_min_u32 s10, s10, s11
	s_max_u32 s14, s14, s10
	s_waitcnt vmcnt(3)
	s_setprio 2
	s_barrier
	v_mfma_f32_16x16x32_f16 v[84:87], v[6:9], v[50:53], v[18:21]
	v_mfma_f32_16x16x32_f16 v[88:91], v[10:13], v[50:53], v[38:41]
	ds_read_b128 v[56:59], v75 offset:0
	ds_read_b128 v[60:63], v75 offset:1024
	v_mfma_f32_16x16x32_f16 v[84:87], v[2:5], v[46:49], v[84:87]
	v_mfma_f32_16x16x32_f16 v[88:91], v[14:17], v[46:49], v[88:91]
	s_waitcnt lgkmcnt(1)
	v_mfma_f32_16x16x32_f16 v[84:87], v[30:33], v[56:59], v[84:87]
	v_mfma_f32_16x16x32_f16 v[88:91], v[22:25], v[56:59], v[88:91]
	s_waitcnt lgkmcnt(0)
	v_mfma_f32_16x16x32_f16 v[84:87], v[34:37], v[60:63], v[84:87]
	v_mfma_f32_16x16x32_f16 v[88:91], v[26:29], v[60:63], v[88:91]
	s_add_u32 s13, s12, 6
	s_min_u32 s13, s13, 450
	s_cmp_ge_u32 s14, s13
	s_cbranch_scc0 .Lca_slow_18
.Lca_ok_16:
	buffer_load_dwordx4 v[46:49], v117, s[4:7], 0 offen offset:3072 sc1
	ds_read_b128 v[50:53], v116 offset:1024
	s_setprio 0
	v_exp_f32_e32 v94, v86
	v_exp_f32_e32 v95, v90
	v_exp_f32_e32 v96, v84
	v_exp_f32_e32 v97, v88
	v_exp_f32_e32 v98, v85
	v_exp_f32_e32 v99, v89
	v_pk_add_f32 v[100:101], v[94:95], 1.0 op_sel_hi:[1,0]
	v_pk_fma_f32 v[102:103], v[94:95], s[8:9], v[92:93] op_sel_hi:[1,0,0]
	v_pk_fma_f32 v[100:101], v[96:97], v[100:101], v[100:101]
	v_pk_fma_f32 v[104:105], v[100:101], v[98:99], v[100:101]
	v_rcp_f32_e32 v104, v104
	v_rcp_f32_e32 v105, v105
	v_pk_fma_f32 v[102:103], v[102:103], v[98:99], v[102:103]
	v_pk_fma_f32 v[102:103], v[64:65], v[100:101], v[102:103]
	v_exp_f32_e32 v106, v87
	v_pk_mul_f32 v[64:65], v[102:103], v[104:105]
	v_exp_f32_e32 v108, v64
	v_exp_f32_e32 v109, v65
	v_exp_f32_e32 v107, v91
	v_pk_add_f32 v[110:111], v[108:109], 1.0 op_sel_hi:[1,0]
	v_pk_fma_f32 v[110:111], v[110:111], v[106:107], v[110:111]
	v_rcp_f32_e32 v110, v110
	v_rcp_f32_e32 v111, v111
	v_pk_add_f32 v[112:113], v[108:109], -1.0 op_sel_hi:[1,0]
	v_pk_mul_f32 v[112:113], v[112:113], v[110:111]
	v_cvt_pk_f16_f32 v114, v112, v113
	ds_write_b32 v81, v114 offset:2048
	s_waitcnt lgkmcnt(0)
	s_waitcnt vmcnt(3)
	s_add_u32 s12, s12, 4
	v_add_u32_e32 v116, 0x400, v116
	v_add_u32_e32 v117, 0x1000, v117
	s_cmp_lt_u32 s12, 450
	s_cbranch_scc1 .Lca_loop
	s_barrier
	s_barrier
	s_barrier
	s_barrier
	s_endpgm
